# baseline (speedup 1.0000x reference)
.LBB1_17:
	v_lshlrev_b32_e32 v2, 16, v167
	v_mov_b32_e32 v3, 0
	v_lshl_add_u64 v[4:5], s[12:13], 0, v[2:3]
	v_mov_b32_e32 v167, v3
	v_lshl_add_u64 v[2:3], v[4:5], 0, v[166:167]
	v_add_co_u32_e32 v4, vcc, 0x4000, v2
	v_cvt_f32_f16_e32 v6, v198
	s_nop 0
	v_addc_co_u32_e32 v5, vcc, 0, v3, vcc
	v_add_co_u32_e32 v6, vcc, 0x8000, v2
	s_movk_i32 s0, 0x1000
	s_nop 0
	v_addc_co_u32_e32 v7, vcc, 0, v3, vcc
	v_add_co_u32_e32 v8, vcc, 0xc000, v2
	s_nop 1
	v_addc_co_u32_e32 v9, vcc, 0, v3, vcc
	global_load_dwordx4 a[224:227], v[2:3], off
	global_load_dwordx4 a[204:207], v[2:3], off offset:1024
	global_load_dwordx4 a[236:239], v[4:5], off
	global_load_dwordx4 a[200:203], v[4:5], off offset:1024
	global_load_dwordx4 a[232:235], v[6:7], off
	global_load_dwordx4 a[196:199], v[6:7], off offset:1024
	global_load_dwordx4 a[228:231], v[8:9], off
	global_load_dwordx4 a[184:187], v[8:9], off offset:1024
	global_load_dwordx4 a[164:167], v[2:3], off offset:2048
	global_load_dwordx4 a[140:143], v[2:3], off offset:3072
	global_load_dwordx4 a[180:183], v[4:5], off offset:2048
	global_load_dwordx4 a[128:131], v[4:5], off offset:3072
	global_load_dwordx4 a[172:175], v[6:7], off offset:2048
	global_load_dwordx4 a[120:123], v[6:7], off offset:3072
	global_load_dwordx4 a[168:171], v[8:9], off offset:2048
	global_load_dwordx4 a[132:135], v[8:9], off offset:3072
	v_add_co_u32_e32 v4, vcc, s0, v2
	s_movk_i32 s0, 0x2000
	s_nop 0
	v_addc_co_u32_e32 v5, vcc, 0, v3, vcc
	v_add_co_u32_e32 v6, vcc, s0, v2
	s_movk_i32 s0, 0x5000
	s_nop 0
	v_addc_co_u32_e32 v7, vcc, 0, v3, vcc
	v_add_co_u32_e32 v8, vcc, s0, v2
	s_movk_i32 s0, 0x6000
	s_nop 0
	v_addc_co_u32_e32 v9, vcc, 0, v3, vcc
	v_add_co_u32_e32 v10, vcc, s0, v2
	s_mov_b32 s0, 0x9000
	s_nop 0
	v_addc_co_u32_e32 v11, vcc, 0, v3, vcc
	v_add_co_u32_e32 v12, vcc, s0, v2
	s_mov_b32 s0, 0xa000
	s_nop 0
	v_addc_co_u32_e32 v13, vcc, 0, v3, vcc
	v_add_co_u32_e32 v14, vcc, s0, v2
	s_mov_b32 s0, 0xd000
	s_nop 0
	v_addc_co_u32_e32 v15, vcc, 0, v3, vcc
	v_add_co_u32_e32 v16, vcc, s0, v2
	s_mov_b32 s0, 0xe000
	s_nop 0
	v_addc_co_u32_e32 v17, vcc, 0, v3, vcc
	v_add_co_u32_e32 v18, vcc, s0, v2
	s_movk_i32 s0, 0x3000
	s_nop 0
	v_addc_co_u32_e32 v19, vcc, 0, v3, vcc
	global_load_dwordx4 a[212:215], v[4:5], off offset:1024
	global_load_dwordx4 a[176:179], v[4:5], off offset:2048
	global_load_dwordx4 a[208:211], v[12:13], off offset:1024
	global_load_dwordx4 a[160:163], v[12:13], off offset:2048
	global_load_dwordx4 a[216:219], v[8:9], off offset:1024
	global_load_dwordx4 a[152:155], v[4:5], off offset:3072
	global_load_dwordx4 a[188:191], v[8:9], off offset:2048
	global_load_dwordx4 a[144:147], v[8:9], off offset:3072
	global_load_dwordx4 a[220:223], v[16:17], off offset:1024
	global_load_dwordx4 a[156:159], v[12:13], off offset:3072
	global_load_dwordx4 a[192:195], v[16:17], off offset:2048
	global_load_dwordx4 a[148:151], v[16:17], off offset:3072
	global_load_dwordx4 a[240:243], v[6:7], off offset:-4096
	global_load_dwordx4 a[124:127], v[6:7], off
	global_load_dwordx4 a[244:247], v[14:15], off offset:-4096
	global_load_dwordx4 a[112:115], v[14:15], off
	global_load_dwordx4 a[136:139], v[10:11], off
	global_load_dwordx4 a[100:103], v[10:11], off offset:1024
	global_load_dwordx4 a[116:119], v[18:19], off
	global_load_dwordx4 a[76:79], v[18:19], off offset:1024
	global_load_dwordx4 a[108:111], v[6:7], off offset:1024
	global_load_dwordx4 a[68:71], v[6:7], off offset:2048
	global_load_dwordx4 a[104:107], v[14:15], off offset:1024
	global_load_dwordx4 a[64:67], v[14:15], off offset:2048
	global_load_dwordx4 a[248:251], v[10:11], off offset:-4096
	global_load_dwordx4 a[48:51], v[6:7], off offset:3072
	global_load_dwordx4 a[80:83], v[10:11], off offset:2048
	global_load_dwordx4 a[40:43], v[10:11], off offset:3072
	global_load_dwordx4 a[252:255], v[18:19], off offset:-4096
	global_load_dwordx4 a[36:39], v[14:15], off offset:3072
	global_load_dwordx4 a[72:75], v[18:19], off offset:2048
	global_load_dwordx4 a[32:35], v[18:19], off offset:3072
	v_add_co_u32_e32 v4, vcc, s0, v2
	s_movk_i32 s0, 0x7000
	s_nop 0
	v_addc_co_u32_e32 v5, vcc, 0, v3, vcc
	v_add_co_u32_e32 v6, vcc, s0, v2
	s_mov_b32 s0, 0xb000
	s_nop 0
	v_addc_co_u32_e32 v7, vcc, 0, v3, vcc
	v_add_co_u32_e32 v8, vcc, s0, v2
	s_mov_b32 s0, 0xf000
	s_nop 0
	v_addc_co_u32_e32 v9, vcc, 0, v3, vcc
	v_add_co_u32_e32 v2, vcc, s0, v2
	s_mov_b32 s0, 0
	s_nop 0
	v_addc_co_u32_e32 v3, vcc, 0, v3, vcc
	global_load_dwordx4 a[84:87], v[4:5], off
	global_load_dwordx4 a[60:63], v[4:5], off offset:1024
	global_load_dwordx4 a[96:99], v[6:7], off
	global_load_dwordx4 a[56:59], v[6:7], off offset:1024
	global_load_dwordx4 a[92:95], v[8:9], off
	global_load_dwordx4 a[52:55], v[8:9], off offset:1024
	global_load_dwordx4 a[88:91], v[2:3], off
	global_load_dwordx4 a[44:47], v[2:3], off offset:1024
	global_load_dwordx4 a[16:19], v[4:5], off offset:2048
	global_load_dwordx4 a[12:15], v[4:5], off offset:3072
	global_load_dwordx4 a[28:31], v[6:7], off offset:2048
	global_load_dwordx4 a[8:11], v[6:7], off offset:3072
	global_load_dwordx4 a[24:27], v[8:9], off offset:2048
	global_load_dwordx4 a[4:7], v[8:9], off offset:3072
	global_load_dwordx4 a[20:23], v[2:3], off offset:2048
	global_load_dwordx4 a[0:3], v[2:3], off offset:3072
	v_cvt_f16_f32_e32 v2, v171
	v_cvt_f16_f32_e32 v7, v170
	v_mul_u32_u24_e32 v4, 0x1080, v201
	v_lshl_add_u32 v4, v202, 1, v4
	v_cvt_f32_f16_e32 v3, v2
	v_or_b32_e32 v5, 0x20000, v4
	s_waitcnt lgkmcnt(0)
	v_sub_f32_e32 v3, v171, v3
	s_mov_b32 s1, 0x45000000
	ds_write_b16 v5, v2
	v_cvt_f32_f16_e32 v5, v7
	v_fma_mixlo_f16 v6, v3, s1, 0
	v_fma_mix_f32 v3, v3, s1, -v6 op_sel_hi:[0,0,1]
	v_add_u32_e32 v2, 0x20420, v4
	v_fma_mixlo_f16 v3, v3, s1, 0
	ds_write_b16 v2, v6
	v_add_u32_e32 v2, 0x20840, v4
	ds_write_b16 v2, v3
	v_sub_f32_e32 v2, v170, v5
	v_cvt_f16_f32_e32 v5, v169
	v_add_u32_e32 v6, 0x20020, v4
	v_fma_mixlo_f16 v3, v2, s1, 0
	ds_write_b16 v6, v7
	v_add_u32_e32 v6, 0x20440, v4
	v_cvt_f32_f16_e32 v7, v5
	ds_write_b16 v6, v3
	v_cvt_f16_f32_e32 v6, v168
	v_fma_mix_f32 v2, v2, s1, -v3 op_sel_hi:[0,0,1]
	v_fma_mixlo_f16 v2, v2, s1, 0
	v_add_u32_e32 v3, 0x20860, v4
	ds_write_b16 v3, v2
	v_sub_f32_e32 v2, v169, v7
	v_add_u32_e32 v7, 0x20040, v4
	ds_write_b16 v7, v5
	v_cvt_f32_f16_e32 v7, v6
	v_fma_mixlo_f16 v3, v2, s1, 0
	v_fma_mix_f32 v2, v2, s1, -v3 op_sel_hi:[0,0,1]
	v_add_u32_e32 v5, 0x20460, v4
	v_fma_mixlo_f16 v2, v2, s1, 0
	ds_write_b16 v5, v3
	v_add_u32_e32 v3, 0x20880, v4
	ds_write_b16 v3, v2
	v_sub_f32_e32 v2, v168, v7
	v_fma_mixlo_f16 v3, v2, s1, 0
	v_add_u32_e32 v5, 0x20060, v4
	v_fma_mix_f32 v2, v2, s1, -v3 op_sel_hi:[0,0,1]
	ds_write_b16 v5, v6
	v_add_u32_e32 v5, 0x20480, v4
	v_fma_mixlo_f16 v2, v2, s1, 0
	ds_write_b16 v5, v3
	v_add_u32_e32 v3, 0x208a0, v4
	s_mov_b32 s2, s0
	s_mov_b32 s3, s0
	v_mul_u32_u24_e32 v18, 0x420, v200
	ds_write_b16 v3, v2
	s_mov_b32 s1, s0
	v_mov_b64_e32 v[16:17], s[2:3]
	v_mov_b64_e32 v[12:13], s[2:3]
	v_mov_b64_e32 v[8:9], s[2:3]
	v_mov_b64_e32 v[4:5], s[2:3]
	v_lshl_add_u32 v22, v203, 1, v18
	v_mov_b64_e32 v[14:15], s[0:1]
	v_mov_b64_e32 v[10:11], s[0:1]
	v_mov_b64_e32 v[6:7], s[0:1]
	v_mov_b64_e32 v[2:3], s[0:1]
	v_or_b32_e32 v18, 0x20000, v22
	s_waitcnt lgkmcnt(0)
	s_barrier
	s_nop 1
	ds_read_b128 v[18:21], v18
	s_waitcnt lgkmcnt(0)
	v_mfma_f32_16x16x32_f16 v[14:17], v[18:21], a[224:227], v[14:17]
	s_waitcnt vmcnt(61)
	v_mfma_f32_16x16x32_f16 v[10:13], v[18:21], a[236:239], v[10:13]
	s_waitcnt vmcnt(59)
	v_mfma_f32_16x16x32_f16 v[6:9], v[18:21], a[232:235], v[6:9]
	s_waitcnt vmcnt(57)
	v_mfma_f32_16x16x32_f16 v[2:5], v[18:21], a[228:231], v[2:5]
	v_add_u32_e32 v18, 0x20040, v22
	ds_read_b128 v[18:21], v18
	s_waitcnt lgkmcnt(0)
	v_mfma_f32_16x16x32_f16 v[14:17], v[18:21], a[204:207], v[14:17]
	v_mfma_f32_16x16x32_f16 v[10:13], v[18:21], a[200:203], v[10:13]
	v_mfma_f32_16x16x32_f16 v[6:9], v[18:21], a[196:199], v[6:9]
	s_waitcnt vmcnt(56)
	v_mfma_f32_16x16x32_f16 v[2:5], v[18:21], a[184:187], v[2:5]
	v_add_u32_e32 v18, 0x20080, v22
	ds_read_b128 v[18:21], v18
	s_waitcnt vmcnt(55) lgkmcnt(0)
	v_mfma_f32_16x16x32_f16 v[14:17], v[18:21], a[164:167], v[14:17]
	s_waitcnt vmcnt(53)
	v_mfma_f32_16x16x32_f16 v[10:13], v[18:21], a[180:183], v[10:13]
	s_waitcnt vmcnt(51)
	v_mfma_f32_16x16x32_f16 v[6:9], v[18:21], a[172:175], v[6:9]
	s_waitcnt vmcnt(49)
	v_mfma_f32_16x16x32_f16 v[2:5], v[18:21], a[168:171], v[2:5]
	v_add_u32_e32 v18, 0x200c0, v22
	ds_read_b128 v[18:21], v18
	s_waitcnt lgkmcnt(0)
	v_mfma_f32_16x16x32_f16 v[14:17], v[18:21], a[140:143], v[14:17]
	v_mfma_f32_16x16x32_f16 v[10:13], v[18:21], a[128:131], v[10:13]
	v_mfma_f32_16x16x32_f16 v[6:9], v[18:21], a[120:123], v[6:9]
	s_waitcnt vmcnt(48)
	v_mfma_f32_16x16x32_f16 v[2:5], v[18:21], a[132:135], v[2:5]
	v_add_u32_e32 v18, 0x20100, v22
	ds_read_b128 v[18:21], v18
	s_waitcnt vmcnt(35) lgkmcnt(0)
	v_mfma_f32_16x16x32_f16 v[14:17], v[18:21], a[240:243], v[14:17]
	s_waitcnt vmcnt(23)
	v_mfma_f32_16x16x32_f16 v[10:13], v[18:21], a[248:251], v[10:13]
	v_mfma_f32_16x16x32_f16 v[6:9], v[18:21], a[244:247], v[6:9]
	s_waitcnt vmcnt(19)
	v_mfma_f32_16x16x32_f16 v[2:5], v[18:21], a[252:255], v[2:5]
	v_add_u32_e32 v18, 0x20140, v22
	ds_read_b128 v[18:21], v18
	s_waitcnt lgkmcnt(0)
	v_mfma_f32_16x16x32_f16 v[14:17], v[18:21], a[212:215], v[14:17]
	v_mfma_f32_16x16x32_f16 v[10:13], v[18:21], a[216:219], v[10:13]
	v_mfma_f32_16x16x32_f16 v[6:9], v[18:21], a[208:211], v[6:9]
	v_mfma_f32_16x16x32_f16 v[2:5], v[18:21], a[220:223], v[2:5]
	v_add_u32_e32 v18, 0x20180, v22
	ds_read_b128 v[18:21], v18
	s_waitcnt lgkmcnt(0)
	v_mfma_f32_16x16x32_f16 v[14:17], v[18:21], a[176:179], v[14:17]
	v_mfma_f32_16x16x32_f16 v[10:13], v[18:21], a[188:191], v[10:13]
	v_mfma_f32_16x16x32_f16 v[6:9], v[18:21], a[160:163], v[6:9]
	v_mfma_f32_16x16x32_f16 v[2:5], v[18:21], a[192:195], v[2:5]
	v_add_u32_e32 v18, 0x201c0, v22
	ds_read_b128 v[18:21], v18
	s_waitcnt lgkmcnt(0)
	v_mfma_f32_16x16x32_f16 v[14:17], v[18:21], a[152:155], v[14:17]
	v_mfma_f32_16x16x32_f16 v[10:13], v[18:21], a[144:147], v[10:13]
	v_mfma_f32_16x16x32_f16 v[6:9], v[18:21], a[156:159], v[6:9]
	v_mfma_f32_16x16x32_f16 v[2:5], v[18:21], a[148:151], v[2:5]
	v_add_u32_e32 v18, 0x20200, v22
	ds_read_b128 v[18:21], v18
	s_waitcnt lgkmcnt(0)
	v_mfma_f32_16x16x32_f16 v[14:17], v[18:21], a[124:127], v[14:17]
	v_mfma_f32_16x16x32_f16 v[10:13], v[18:21], a[136:139], v[10:13]
	v_mfma_f32_16x16x32_f16 v[6:9], v[18:21], a[112:115], v[6:9]
	v_mfma_f32_16x16x32_f16 v[2:5], v[18:21], a[116:119], v[2:5]
	v_add_u32_e32 v18, 0x20240, v22
	ds_read_b128 v[18:21], v18
	s_waitcnt lgkmcnt(0)
	v_mfma_f32_16x16x32_f16 v[14:17], v[18:21], a[108:111], v[14:17]
	v_mfma_f32_16x16x32_f16 v[10:13], v[18:21], a[100:103], v[10:13]
	v_mfma_f32_16x16x32_f16 v[6:9], v[18:21], a[104:107], v[6:9]
	v_mfma_f32_16x16x32_f16 v[2:5], v[18:21], a[76:79], v[2:5]
	v_add_u32_e32 v18, 0x20280, v22
	ds_read_b128 v[18:21], v18
	s_waitcnt lgkmcnt(0)
	v_mfma_f32_16x16x32_f16 v[14:17], v[18:21], a[68:71], v[14:17]
	v_mfma_f32_16x16x32_f16 v[10:13], v[18:21], a[80:83], v[10:13]
	v_mfma_f32_16x16x32_f16 v[6:9], v[18:21], a[64:67], v[6:9]
	s_waitcnt vmcnt(17)
	v_mfma_f32_16x16x32_f16 v[2:5], v[18:21], a[72:75], v[2:5]
	v_add_u32_e32 v18, 0x202c0, v22
	ds_read_b128 v[18:21], v18
	s_waitcnt lgkmcnt(0)
	v_mfma_f32_16x16x32_f16 v[14:17], v[18:21], a[48:51], v[14:17]
	v_mfma_f32_16x16x32_f16 v[10:13], v[18:21], a[40:43], v[10:13]
	v_mfma_f32_16x16x32_f16 v[6:9], v[18:21], a[36:39], v[6:9]
	s_waitcnt vmcnt(16)
	v_mfma_f32_16x16x32_f16 v[2:5], v[18:21], a[32:35], v[2:5]
	v_add_u32_e32 v18, 0x20300, v22
	ds_read_b128 v[18:21], v18
	s_waitcnt vmcnt(15) lgkmcnt(0)
	v_mfma_f32_16x16x32_f16 v[14:17], v[18:21], a[84:87], v[14:17]
	s_waitcnt vmcnt(13)
	v_mfma_f32_16x16x32_f16 v[10:13], v[18:21], a[96:99], v[10:13]
	s_waitcnt vmcnt(11)
	v_mfma_f32_16x16x32_f16 v[6:9], v[18:21], a[92:95], v[6:9]
	s_waitcnt vmcnt(9)
	v_mfma_f32_16x16x32_f16 v[2:5], v[18:21], a[88:91], v[2:5]
	v_add_u32_e32 v18, 0x20340, v22
	ds_read_b128 v[18:21], v18
	s_waitcnt lgkmcnt(0)
	v_mfma_f32_16x16x32_f16 v[14:17], v[18:21], a[60:63], v[14:17]
	v_mfma_f32_16x16x32_f16 v[10:13], v[18:21], a[56:59], v[10:13]
	v_mfma_f32_16x16x32_f16 v[6:9], v[18:21], a[52:55], v[6:9]
	s_waitcnt vmcnt(8)
	v_mfma_f32_16x16x32_f16 v[2:5], v[18:21], a[44:47], v[2:5]
	v_add_u32_e32 v18, 0x20380, v22
	ds_read_b128 v[18:21], v18
	s_waitcnt vmcnt(7) lgkmcnt(0)
	v_mfma_f32_16x16x32_f16 v[14:17], v[18:21], a[16:19], v[14:17]
	s_waitcnt vmcnt(5)
	v_mfma_f32_16x16x32_f16 v[10:13], v[18:21], a[28:31], v[10:13]
	s_waitcnt vmcnt(3)
	v_mfma_f32_16x16x32_f16 v[6:9], v[18:21], a[24:27], v[6:9]
	s_waitcnt vmcnt(1)
	v_mfma_f32_16x16x32_f16 v[2:5], v[18:21], a[20:23], v[2:5]
	v_add_u32_e32 v18, 0x203c0, v22
	ds_read_b128 v[18:21], v18
	s_waitcnt lgkmcnt(0)
	v_mfma_f32_16x16x32_f16 v[14:17], v[18:21], a[12:15], v[14:17]
	v_mfma_f32_16x16x32_f16 v[10:13], v[18:21], a[8:11], v[10:13]
	v_mfma_f32_16x16x32_f16 v[6:9], v[18:21], a[4:7], v[6:9]
	s_waitcnt vmcnt(0)
	v_mfma_f32_16x16x32_f16 v[2:5], v[18:21], a[0:3], v[2:5]
	v_cmp_gt_u32_e32 vcc, 32, v1
	s_nop 15
	s_and_saveexec_b64 s[0:1], vcc
	s_cbranch_execz .LBB1_19
	v_lshlrev_b32_e32 v1, 6, v0
	s_movk_i32 s2, 0xc0
	v_and_b32_e32 v1, 0x400, v1
	v_and_or_b32 v5, v0, s2, v179
	v_lshl_or_b32 v1, v5, 2, v1
	v_fmamk_f32 v5, v15, 0x3a000000, v14
	v_fmamk_f32 v9, v11, 0x3a000000, v10
	v_fmac_f32_e32 v5, 0x34800000, v16
	v_fmac_f32_e32 v9, 0x34800000, v12
	ds_write2_b32 v1, v5, v9 offset1:16
	v_fmamk_f32 v5, v7, 0x3a000000, v6
	v_fmamk_f32 v2, v3, 0x3a000000, v2
	v_fmac_f32_e32 v5, 0x34800000, v8
	v_fmac_f32_e32 v2, 0x34800000, v4
	ds_write2_b32 v1, v5, v2 offset0:32 offset1:48
